# code placement scan: both attention main loops at byte phase 0 mod 64
# baseline (speedup 1.0000x reference)
.LBB0_259:
	s_add_i32 s21, s21, 1
	s_cmp_eq_u32 s21, 4
	s_cbranch_scc1 .LBB0_349
	s_nop 0
	s_nop 0
	s_nop 0
	s_nop 0
	s_nop 0
	s_nop 0
	s_nop 0
	s_nop 0
	s_nop 0
	s_nop 0
	s_nop 0
	s_nop 0

.LBB0_346:
	v_max_f32_e32 v16, v16, v16
	v_max_f32_e32 v17, 0, v16
	v_exp_f32_e64 v16, -v17
	v_cmp_gt_u32_e32 vcc, 32, v230
	s_and_saveexec_b64 s[2:3], vcc
	ds_write_b32 v235, v16
	s_or_b64 exec, exec, s[2:3]
	v_sub_f32_e32 v113, v113, v17
	v_sub_f32_e32 v112, v112, v17
	v_sub_f32_e32 v111, v111, v17
	v_sub_f32_e32 v110, v110, v17
	v_sub_f32_e32 v109, v109, v17
	v_sub_f32_e32 v108, v108, v17
	v_sub_f32_e32 v107, v107, v17
	v_sub_f32_e32 v106, v106, v17
	v_sub_f32_e32 v105, v105, v17
	v_sub_f32_e32 v104, v104, v17
	v_sub_f32_e32 v103, v103, v17
	v_sub_f32_e32 v102, v102, v17
	v_sub_f32_e32 v101, v101, v17
	v_sub_f32_e32 v100, v100, v17
	v_sub_f32_e32 v99, v99, v17
	v_sub_f32_e32 v98, v98, v17
	v_sub_f32_e32 v97, v97, v17
	v_sub_f32_e32 v96, v96, v17
	v_sub_f32_e32 v95, v95, v17
	v_sub_f32_e32 v94, v94, v17
	v_sub_f32_e32 v93, v93, v17
	v_sub_f32_e32 v92, v92, v17
	v_sub_f32_e32 v91, v91, v17
	v_sub_f32_e32 v90, v90, v17
	v_sub_f32_e32 v89, v89, v17
	v_sub_f32_e32 v88, v88, v17
	v_sub_f32_e32 v87, v87, v17
	v_sub_f32_e32 v86, v86, v17
	v_sub_f32_e32 v85, v85, v17
	v_sub_f32_e32 v84, v84, v17
	v_sub_f32_e32 v83, v83, v17
	v_sub_f32_e32 v82, v82, v17
	v_mul_f32_e32 v243, v243, v16
	s_branch .LBB0_340
	s_nop 0
	s_nop 0
	s_nop 0
	s_nop 0
.LBB0_349:
	v_mov_b32_e32 v52, v0
	s_barrier
	s_ashr_i32 s21, s20, 31
	v_readfirstlane_b32 s0, v52
	s_ashr_i32 s2, s0, 2
	s_and_b32 s36, s2, -16
	s_ashr_i32 s3, s0, 7
	v_lshlrev_b32_e32 v2, 4, v52
	v_and_b32_e32 v38, 48, v52
	v_mov_b32_e32 v39, 0
	v_and_b32_e32 v59, 48, v2
	v_lshl_add_u64 v[2:3], s[22:23], 0, v[38:39]
	s_mov_b64 s[0:1], 0x100000
	s_cmp_gt_i32 s3, -1
	v_lshl_add_u64 v[42:43], v[2:3], 0, s[0:1]
	s_cselect_b64 s[0:1], -1, 0
	s_cmp_gt_i32 s3, 0
	v_ashrrev_i32_e32 v58, 2, v52
	s_cselect_b64 s[24:25], -1, 0
	s_cmp_gt_i32 s3, 1
	s_movk_i32 s4, 0x1200
	v_and_b32_e32 v1, 63, v52
	s_cselect_b64 s[26:27], -1, 0
	s_cmp_gt_i32 s3, 2
	v_bfi_b32 v44, -16, s2, v52
	v_mad_i64_i32 v[2:3], s[2:3], v58, s4, 0
	v_mov_b32_e32 v8, 0x90000
	v_lshlrev_b32_e32 v1, 2, v1
	v_mad_i64_i32 v[2:3], s[2:3], s20, v8, v[2:3]
	v_xor_b32_e32 v45, 4, v1
	v_xor_b32_e32 v53, 8, v1
	s_cselect_b64 s[28:29], -1, 0
	v_and_b32_e32 v1, 3, v52
	s_add_u32 s2, s94, s41
	v_lshl_or_b32 v2, v1, 5, v2
	s_addc_u32 s3, s95, 0
	v_bfe_u32 v41, v52, 4, 2
	v_lshl_add_u64 v[46:47], s[2:3], 0, v[2:3]
	v_mad_i64_i32 v[2:3], s[4:5], v44, s4, 0
	v_lshlrev_b32_e32 v40, 3, v41
	v_mad_i64_i32 v[2:3], s[4:5], s20, v8, v[2:3]
	v_or_b32_e32 v2, v2, v40
	v_and_b32_e32 v55, 15, v52
	v_lshl_add_u64 v[2:3], s[2:3], 0, v[2:3]
	s_mov_b64 s[2:3], 0x10a00040
	v_lshl_add_u32 v4, v58, 1, 0
	v_add_u32_e32 v5, 0, v38
	v_mul_u32_u24_e32 v6, 0x110, v59
	v_mul_u32_u24_e32 v7, 0x110, v55
	v_lshl_add_u64 v[48:49], v[2:3], 0, s[2:3]
	v_cndmask_b32_e64 v2, 0, 1, s[0:1]
	s_mov_b64 s[30:31], 0
	s_mov_b64 s[34:35], 0x10a00200
	v_mov_b32_e32 v39, 0x3727c5ac
	s_mov_b32 s33, 0xf800000
	v_mov_b32_e32 v54, 0x260
	s_movk_i32 s37, 0x7fff
	v_add_u32_e32 v56, v4, v6
	v_cmp_ne_u32_e64 s[2:3], 1, v2
	v_add_u32_e32 v57, v5, v7
	v_mov_b32_e32 v60, 1
	v_readlane_b32 s41, v254, 39
	s_branch .LBB0_351

.LBB0_872:
	s_add_i32 s21, s21, 1
	s_cmp_eq_u32 s21, 4
	s_cbranch_scc1 .LBB0_962
	s_nop 0
	s_nop 0
	s_nop 0
	s_nop 0
	s_nop 0
	s_nop 0
	s_nop 0
	s_nop 0
	s_nop 0
	s_nop 0
	s_nop 0

.LBB0_955:
	s_cmp_lg_u32 0, -1
	s_cselect_b32 s0, 0, 0
	s_addk_i32 s0, 0x6000
	v_add3_u32 v8, v237, s0, v233
	s_add_i32 s0, s43, 0x4000
	v_add_f32_e32 v2, v243, v2
	s_and_b32 s0, s0, 0xffff
	v_add3_u32 v16, v8, v236, s0
	ds_read_b64_tr_b16 v[8:9],v16 offset:0
	ds_read_b64_tr_b16 v[10:11],v16 offset:512
	ds_read_b64_tr_b16 v[12:13],v16 offset:1024
	ds_read_b64_tr_b16 v[14:15],v16 offset:1536
	ds_read_b64_tr_b16 v[82:83],v16 offset:2048
	ds_read_b64_tr_b16 v[84:85],v16 offset:2560
	ds_read_b64_tr_b16 v[86:87],v16 offset:3072
	ds_read_b64_tr_b16 v[88:89],v16 offset:3584
	s_waitcnt lgkmcnt(0)
	s_nop 0
	v_mfma_f32_32x32x16_bf16 v[66:81], v[138:141], v[8:11], v[66:81]
	ds_read_b64_tr_b16 v[8:9],v16 offset:4096
	ds_read_b64_tr_b16 v[10:11],v16 offset:4608
	v_mfma_f32_32x32x16_bf16 v[66:81], v[134:137], v[12:15], v[66:81]
	ds_read_b64_tr_b16 v[12:13],v16 offset:5120
	ds_read_b64_tr_b16 v[14:15],v16 offset:5632
	v_mfma_f32_32x32x16_bf16 v[66:81], v[130:133], v[82:85], v[66:81]
	ds_read_b64_tr_b16 v[82:83],v16 offset:6144
	ds_read_b64_tr_b16 v[84:85],v16 offset:6656
	ds_read_b64_tr_b16 v[90:91],v16 offset:7168
	ds_read_b64_tr_b16 v[92:93],v16 offset:7680
	s_waitcnt lgkmcnt(0)
	v_mfma_f32_32x32x16_bf16 v[66:81], v[4:7], v[86:89], v[66:81]
	v_mfma_f32_32x32x16_bf16 v[50:65], v[138:141], v[8:11], v[50:65]
	v_add_u32_e32 v16, 0x2000, v16
	ds_read_b64_tr_b16 v[8:9],v16 offset:0
	ds_read_b64_tr_b16 v[10:11],v16 offset:512
	v_mfma_f32_32x32x16_bf16 v[50:65], v[134:137], v[12:15], v[50:65]
	ds_read_b64_tr_b16 v[12:13],v16 offset:1024
	ds_read_b64_tr_b16 v[14:15],v16 offset:1536
	v_mfma_f32_32x32x16_bf16 v[50:65], v[130:133], v[82:85], v[50:65]
	ds_read_b64_tr_b16 v[82:83],v16 offset:2048
	ds_read_b64_tr_b16 v[84:85],v16 offset:2560
	ds_read_b64_tr_b16 v[86:87],v16 offset:3072
	ds_read_b64_tr_b16 v[88:89],v16 offset:3584
	s_waitcnt lgkmcnt(0)
	v_mfma_f32_32x32x16_bf16 v[50:65], v[4:7], v[90:93], v[50:65]
	v_mfma_f32_32x32x16_bf16 v[34:49], v[138:141], v[8:11], v[34:49]
	ds_read_b64_tr_b16 v[8:9],v16 offset:4096
	ds_read_b64_tr_b16 v[10:11],v16 offset:4608
	v_mfma_f32_32x32x16_bf16 v[34:49], v[134:137], v[12:15], v[34:49]
	ds_read_b64_tr_b16 v[12:13],v16 offset:5120
	ds_read_b64_tr_b16 v[14:15],v16 offset:5632
	v_mfma_f32_32x32x16_bf16 v[34:49], v[130:133], v[82:85], v[34:49]
	ds_read_b64_tr_b16 v[82:83],v16 offset:6144
	ds_read_b64_tr_b16 v[84:85],v16 offset:6656
	ds_read_b64_tr_b16 v[90:91],v16 offset:7168
	ds_read_b64_tr_b16 v[92:93],v16 offset:7680
	s_waitcnt lgkmcnt(0)
	v_mfma_f32_32x32x16_bf16 v[34:49], v[4:7], v[86:89], v[34:49]
	v_mfma_f32_32x32x16_bf16 v[18:33], v[138:141], v[8:11], v[18:33]
	v_mov_b32_e32 v8, v2
	s_nop 1
	v_permlane32_swap_b32_e32 v2, v8
	v_cmp_gt_u32_e32 vcc, 32, v230
	v_mfma_f32_32x32x16_bf16 v[18:33], v[134:137], v[12:15], v[18:33]
	v_mfma_f32_32x32x16_bf16 v[18:33], v[130:133], v[82:85], v[18:33]
	v_mfma_f32_32x32x16_bf16 v[18:33], v[4:7], v[90:93], v[18:33]
	s_and_saveexec_b64 s[0:1], vcc
	v_add_f32_e32 v2, v2, v8
	ds_write_b32 v235, v2 offset:128
	s_or_b64 exec, exec, s[0:1]
	s_waitcnt lgkmcnt(0)
	ds_read_b128 v[4:7], v234 offset:128
	ds_read_b128 v[8:11], v234 offset:160
	s_lshl_b32 s0, s42, 8
	s_add_u32 s2, s6, s0
	s_addc_u32 s3, s7, 0
	s_waitcnt lgkmcnt(1)
	v_rcp_f32_e32 v14, v4
	v_rcp_f32_e32 v15, v5
	v_rcp_f32_e32 v16, v6
	v_rcp_f32_e32 v17, v7
	ds_read_b128 v[4:7], v234 offset:192
	s_lshl_b64 s[0:1], s[26:27], 11
	s_add_u32 s0, s2, s0
	s_addc_u32 s1, s3, s1
	s_lshl_b32 s2, s33, 12
	s_add_i32 s2, s2, 0
	v_lshlrev_b32_e32 v2, 1, v232
	s_add_i32 s2, s2, 0x16800
	v_and_b32_e32 v2, 0x70, v2
	s_waitcnt lgkmcnt(1)
	v_rcp_f32_e32 v82, v8
	v_rcp_f32_e32 v83, v9
	v_rcp_f32_e32 v84, v10
	v_rcp_f32_e32 v85, v11
	ds_read_b128 v[8:11], v234 offset:224
	s_waitcnt lgkmcnt(1)
	v_rcp_f32_e32 v86, v4
	v_lshlrev_b32_e32 v4, 1, v231
	v_add_u32_e32 v95, s2, v2
	v_lshl_add_u64 v[12:13], s[0:1], 0, v[2:3]
	v_lshlrev_b32_e32 v2, 9, v229
	v_add3_u32 v97, s2, v4, v2
	v_mul_f32_e32 v2, v66, v14
	v_cvt_pk_bf16_f32 v2, v2, s0
	ds_write_b16 v97, v2
	v_mul_f32_e32 v2, v50, v14
	v_cvt_pk_bf16_f32 v2, v2, s0
	ds_write_b16 v97, v2 offset:64
	v_mul_f32_e32 v2, v67, v15
	v_cvt_pk_bf16_f32 v2, v2, s0
	ds_write_b16 v97, v2 offset:128
	v_mul_f32_e32 v2, v51, v15
	v_cvt_pk_bf16_f32 v2, v2, s0
	ds_write_b16 v97, v2 offset:192
	v_mul_f32_e32 v2, v68, v16
	v_cvt_pk_bf16_f32 v2, v2, s0
	ds_write_b16 v97, v2 offset:256
	v_mul_f32_e32 v2, v52, v16
	v_cvt_pk_bf16_f32 v2, v2, s0
	ds_write_b16 v97, v2 offset:320
	v_mul_f32_e32 v2, v69, v17
	v_cvt_pk_bf16_f32 v2, v2, s0
	ds_write_b16 v97, v2 offset:384
	v_mul_f32_e32 v2, v53, v17
	v_cvt_pk_bf16_f32 v2, v2, s0
	ds_write_b16 v97, v2 offset:448
	v_mul_f32_e32 v2, v70, v82
	v_cvt_pk_bf16_f32 v2, v2, s0
	ds_write_b16 v97, v2 offset:1024
	v_mul_f32_e32 v2, v54, v82
	v_cvt_pk_bf16_f32 v2, v2, s0
	ds_write_b16 v97, v2 offset:1088
	v_mul_f32_e32 v2, v71, v83
	v_cvt_pk_bf16_f32 v2, v2, s0
	ds_write_b16 v97, v2 offset:1152
	v_mul_f32_e32 v2, v55, v83
	v_cvt_pk_bf16_f32 v2, v2, s0
	ds_write_b16 v97, v2 offset:1216
	v_mul_f32_e32 v2, v72, v84
	v_cvt_pk_bf16_f32 v2, v2, s0
	ds_write_b16 v97, v2 offset:1280
	v_mul_f32_e32 v2, v56, v84
	v_cvt_pk_bf16_f32 v2, v2, s0
	ds_write_b16 v97, v2 offset:1344
	v_mul_f32_e32 v2, v73, v85
	v_cvt_pk_bf16_f32 v2, v2, s0
	ds_write_b16 v97, v2 offset:1408
	v_mul_f32_e32 v2, v57, v85
	v_cvt_pk_bf16_f32 v2, v2, s0
	v_rcp_f32_e32 v87, v5
	ds_write_b16 v97, v2 offset:1472
	v_mul_f32_e32 v2, v74, v86
	v_cvt_pk_bf16_f32 v2, v2, s0
	ds_write_b16 v97, v2 offset:2048
	v_mul_f32_e32 v2, v58, v86
	v_cvt_pk_bf16_f32 v2, v2, s0
	v_rcp_f32_e32 v88, v6
	ds_write_b16 v97, v2 offset:2112
	v_mul_f32_e32 v2, v75, v87
	v_cvt_pk_bf16_f32 v2, v2, s0
	ds_write_b16 v97, v2 offset:2176
	v_mul_f32_e32 v2, v59, v87
	v_cvt_pk_bf16_f32 v2, v2, s0
	v_rcp_f32_e32 v89, v7
	ds_write_b16 v97, v2 offset:2240
	v_mul_f32_e32 v2, v76, v88
	v_cvt_pk_bf16_f32 v2, v2, s0
	ds_write_b16 v97, v2 offset:2304
	v_mul_f32_e32 v2, v60, v88
	v_cvt_pk_bf16_f32 v2, v2, s0
	s_waitcnt lgkmcnt(14)
	v_rcp_f32_e32 v90, v8
	ds_write_b16 v97, v2 offset:2368
	v_mul_f32_e32 v2, v77, v89
	v_cvt_pk_bf16_f32 v2, v2, s0
	ds_write_b16 v97, v2 offset:2432
	v_mul_f32_e32 v2, v61, v89
	v_cvt_pk_bf16_f32 v2, v2, s0
	v_rcp_f32_e32 v91, v9
	ds_write_b16 v97, v2 offset:2496
	v_mul_f32_e32 v2, v78, v90
	v_cvt_pk_bf16_f32 v2, v2, s0
	ds_write_b16 v97, v2 offset:3072
	v_mul_f32_e32 v2, v62, v90
	v_cvt_pk_bf16_f32 v2, v2, s0
	v_rcp_f32_e32 v92, v10
	ds_write_b16 v97, v2 offset:3136
	v_mul_f32_e32 v2, v79, v91
	v_cvt_pk_bf16_f32 v2, v2, s0
	ds_write_b16 v97, v2 offset:3200
	v_mul_f32_e32 v2, v63, v91
	v_cvt_pk_bf16_f32 v2, v2, s0
	v_rcp_f32_e32 v93, v11
	ds_write_b16 v97, v2 offset:3264
	v_mul_f32_e32 v2, v80, v92
	v_cvt_pk_bf16_f32 v2, v2, s0
	ds_write_b16 v97, v2 offset:3328
	v_mul_f32_e32 v2, v64, v92
	v_cvt_pk_bf16_f32 v2, v2, s0
	ds_write_b16 v97, v2 offset:3392
	v_mul_f32_e32 v2, v81, v93
	v_cvt_pk_bf16_f32 v2, v2, s0
	ds_write_b16 v97, v2 offset:3456
	v_mul_f32_e32 v2, v65, v93
	v_lshrrev_b32_e32 v94, 3, v230
	v_cvt_pk_bf16_f32 v2, v2, s0
	ds_write_b16 v97, v2 offset:3520
	v_or_b32_e32 v52, 8, v94
	v_lshl_add_u32 v96, v94, 7, v95
	s_waitcnt lgkmcnt(0)
	v_lshl_add_u32 v58, v52, 7, v95
	ds_read_b128 v[4:7], v96
	ds_read_b128 v[8:11], v58
	v_lshlrev_b32_e32 v2, 11, v94
	v_lshl_add_u64 v[50:51], v[12:13], 0, v[2:3]
	v_lshlrev_b32_e32 v2, 11, v52
	v_lshl_add_u64 v[52:53], v[12:13], 0, v[2:3]
	v_or_b32_e32 v2, 16, v94
	v_or_b32_e32 v56, 24, v94
	v_lshl_add_u32 v59, v2, 7, v95
	v_lshl_add_u32 v60, v56, 7, v95
	s_waitcnt lgkmcnt(1)
	global_store_dwordx4 v[50:51], v[4:7], off
	ds_read_b128 v[4:7], v59
	s_waitcnt lgkmcnt(1)
	global_store_dwordx4 v[52:53], v[8:11], off
	ds_read_b128 v[8:11], v60
	v_lshlrev_b32_e32 v2, 11, v2
	v_lshl_add_u64 v[54:55], v[12:13], 0, v[2:3]
	v_lshlrev_b32_e32 v2, 11, v56
	v_lshl_add_u64 v[56:57], v[12:13], 0, v[2:3]
	v_mul_f32_e32 v2, v34, v14
	s_waitcnt lgkmcnt(1)
	global_store_dwordx4 v[54:55], v[4:7], off
	s_waitcnt lgkmcnt(0)
	global_store_dwordx4 v[56:57], v[8:11], off
	v_cvt_pk_bf16_f32 v2, v2, s0
	s_waitcnt lgkmcnt(0)
	ds_write_b16 v97, v2
	v_mul_f32_e32 v2, v18, v14
	v_cvt_pk_bf16_f32 v2, v2, s0
	ds_write_b16 v97, v2 offset:64
	v_mul_f32_e32 v2, v35, v15
	v_cvt_pk_bf16_f32 v2, v2, s0
	ds_write_b16 v97, v2 offset:128
	v_mul_f32_e32 v2, v19, v15
	v_cvt_pk_bf16_f32 v2, v2, s0
	ds_write_b16 v97, v2 offset:192
	v_mul_f32_e32 v2, v36, v16
	v_cvt_pk_bf16_f32 v2, v2, s0
	ds_write_b16 v97, v2 offset:256
	v_mul_f32_e32 v2, v20, v16
	v_cvt_pk_bf16_f32 v2, v2, s0
	ds_write_b16 v97, v2 offset:320
	v_mul_f32_e32 v2, v37, v17
	v_cvt_pk_bf16_f32 v2, v2, s0
	ds_write_b16 v97, v2 offset:384
	v_mul_f32_e32 v2, v21, v17
	v_cvt_pk_bf16_f32 v2, v2, s0
	ds_write_b16 v97, v2 offset:448
	v_mul_f32_e32 v2, v38, v82
	v_cvt_pk_bf16_f32 v2, v2, s0
	ds_write_b16 v97, v2 offset:1024
	v_mul_f32_e32 v2, v22, v82
	v_cvt_pk_bf16_f32 v2, v2, s0
	ds_write_b16 v97, v2 offset:1088
	v_mul_f32_e32 v2, v39, v83
	v_cvt_pk_bf16_f32 v2, v2, s0
	ds_write_b16 v97, v2 offset:1152
	v_mul_f32_e32 v2, v23, v83
	v_cvt_pk_bf16_f32 v2, v2, s0
	ds_write_b16 v97, v2 offset:1216
	v_mul_f32_e32 v2, v40, v84
	v_cvt_pk_bf16_f32 v2, v2, s0
	ds_write_b16 v97, v2 offset:1280
	v_mul_f32_e32 v2, v24, v84
	v_cvt_pk_bf16_f32 v2, v2, s0
	ds_write_b16 v97, v2 offset:1344
	v_mul_f32_e32 v2, v41, v85
	v_cvt_pk_bf16_f32 v2, v2, s0
	ds_write_b16 v97, v2 offset:1408
	v_mul_f32_e32 v2, v25, v85
	v_cvt_pk_bf16_f32 v2, v2, s0
	ds_write_b16 v97, v2 offset:1472
	v_mul_f32_e32 v2, v42, v86
	v_cvt_pk_bf16_f32 v2, v2, s0
	ds_write_b16 v97, v2 offset:2048
	v_mul_f32_e32 v2, v26, v86
	v_cvt_pk_bf16_f32 v2, v2, s0
	ds_write_b16 v97, v2 offset:2112
	v_mul_f32_e32 v2, v43, v87
	v_cvt_pk_bf16_f32 v2, v2, s0
	ds_write_b16 v97, v2 offset:2176
	v_mul_f32_e32 v2, v27, v87
	v_cvt_pk_bf16_f32 v2, v2, s0
	ds_write_b16 v97, v2 offset:2240
	v_mul_f32_e32 v2, v44, v88
	v_cvt_pk_bf16_f32 v2, v2, s0
	ds_write_b16 v97, v2 offset:2304
	v_mul_f32_e32 v2, v28, v88
	v_cvt_pk_bf16_f32 v2, v2, s0
	ds_write_b16 v97, v2 offset:2368
	v_mul_f32_e32 v2, v45, v89
	v_cvt_pk_bf16_f32 v2, v2, s0
	ds_write_b16 v97, v2 offset:2432
	v_mul_f32_e32 v2, v29, v89
	v_cvt_pk_bf16_f32 v2, v2, s0
	ds_write_b16 v97, v2 offset:2496
	v_mul_f32_e32 v2, v46, v90
	v_cvt_pk_bf16_f32 v2, v2, s0
	ds_write_b16 v97, v2 offset:3072
	v_mul_f32_e32 v2, v30, v90
	v_cvt_pk_bf16_f32 v2, v2, s0
	ds_write_b16 v97, v2 offset:3136
	v_mul_f32_e32 v2, v47, v91
	v_cvt_pk_bf16_f32 v2, v2, s0
	ds_write_b16 v97, v2 offset:3200
	v_mul_f32_e32 v2, v31, v91
	v_cvt_pk_bf16_f32 v2, v2, s0
	ds_write_b16 v97, v2 offset:3264
	v_mul_f32_e32 v2, v48, v92
	v_cvt_pk_bf16_f32 v2, v2, s0
	ds_write_b16 v97, v2 offset:3328
	v_mul_f32_e32 v2, v32, v92
	v_cvt_pk_bf16_f32 v2, v2, s0
	ds_write_b16 v97, v2 offset:3392
	v_mul_f32_e32 v2, v49, v93
	v_cvt_pk_bf16_f32 v2, v2, s0
	ds_write_b16 v97, v2 offset:3456
	v_mul_f32_e32 v2, v33, v93
	v_cvt_pk_bf16_f32 v2, v2, s0
	ds_write_b16 v97, v2 offset:3520
	s_waitcnt lgkmcnt(0)
	ds_read_b128 v[4:7], v96
	ds_read_b128 v[8:11], v58
	ds_read_b128 v[12:15], v59
	ds_read_b128 v[16:19], v60
	s_waitcnt lgkmcnt(3)
	global_store_dwordx4 v[50:51], v[4:7], off offset:128
	s_waitcnt lgkmcnt(2)
	global_store_dwordx4 v[52:53], v[8:11], off offset:128
	s_waitcnt lgkmcnt(1)
	global_store_dwordx4 v[54:55], v[12:15], off offset:128
	s_waitcnt lgkmcnt(0)
	global_store_dwordx4 v[56:57], v[16:19], off offset:128
	s_waitcnt lgkmcnt(0)
	s_waitcnt lgkmcnt(0)
	s_barrier
	s_cmp_lt_u32 s21, 2
	s_cbranch_scc1 .LBB0_872
	v_mov_b32_e32 v6, v0
	s_lshl_b32 s0, s63, 8
	v_ashrrev_i32_e32 v4, 1, v6
	s_or_b32 s0, s8, s0
	s_mov_b32 s1, s9
	v_ashrrev_i32_e32 v5, 31, v4
	v_lshl_add_u64 v[12:13], s[0:1], 0, v[4:5]
	v_lshlrev_b32_e32 v2, 6, v6
	v_lshlrev_b64 v[4:5], 11, v[12:13]
	v_and_b32_e32 v7, 64, v2
	v_lshl_add_u64 v[4:5], s[6:7], 0, v[4:5]
	v_lshlrev_b32_e32 v2, 1, v7
	v_lshl_add_u64 v[4:5], v[4:5], 0, v[2:3]
	s_waitcnt vmcnt(0)
	s_barrier
	global_load_dwordx2 v[16:17], v[4:5], off sc1
	global_load_dwordx2 v[18:19], v[4:5], off offset:256 sc1
	global_load_dwordx2 v[24:25], v[4:5], off offset:8 sc1
	global_load_dwordx2 v[26:27], v[4:5], off offset:264 sc1
	global_load_dwordx2 v[30:31], v[4:5], off offset:16 sc1
	global_load_dwordx2 v[34:35], v[4:5], off offset:272 sc1
	global_load_dwordx2 v[42:43], v[4:5], off offset:24 sc1
	global_load_dwordx2 v[50:51], v[4:5], off offset:280 sc1
	v_lshlrev_b32_e32 v6, 2, v6
	v_bitop3_b32 v83, v6, 4, v228 bitop3:0x6c
	v_lshlrev_b32_e32 v82, 2, v7
	global_load_dwordx2 v[54:55], v[4:5], off offset:32 sc1
	global_load_dwordx2 v[60:61], v[4:5], off offset:288 sc1
	global_load_dwordx2 v[74:75], v[4:5], off offset:40 sc1
	global_load_dwordx2 v[84:85], v[4:5], off offset:296 sc1
	global_load_dwordx2 v[86:87], v[4:5], off offset:48 sc1
	global_load_dwordx2 v[88:89], v[4:5], off offset:304 sc1
	global_load_dwordx2 v[90:91], v[4:5], off offset:56 sc1
	global_load_dwordx2 v[28:29], v[4:5], off offset:312 sc1
	global_load_dwordx2 v[58:59], v[4:5], off offset:64 sc1
	global_load_dwordx2 v[36:37], v[4:5], off offset:320 sc1
	global_load_dwordx2 v[66:67], v[4:5], off offset:72 sc1
	global_load_dwordx2 v[44:45], v[4:5], off offset:328 sc1
	global_load_dwordx2 v[62:63], v[4:5], off offset:80 sc1
	global_load_dwordx2 v[52:53], v[4:5], off offset:336 sc1
	global_load_dwordx2 v[76:77], v[4:5], off offset:88 sc1
	global_load_dwordx2 v[32:33], v[4:5], off offset:344 sc1
	global_load_dwordx2 v[68:69], v[4:5], off offset:96 sc1
	global_load_dwordx2 v[38:39], v[4:5], off offset:352 sc1
	global_load_dwordx2 v[80:81], v[4:5], off offset:104 sc1
	global_load_dwordx2 v[20:21], v[4:5], off offset:360 sc1
	global_load_dwordx2 v[46:47], v[4:5], off offset:112 sc1
	global_load_dwordx2 v[22:23], v[4:5], off offset:368 sc1
	global_load_dwordx2 v[56:57], v[4:5], off offset:120 sc1
	global_load_dwordx2 v[48:49], v[4:5], off offset:376 sc1
	s_nop 0
	global_load_dwordx4 v[4:7], v82, s[58:59] offset:528
	global_load_dwordx4 v[8:11], v82, s[58:59] offset:512
	v_mov_b64_e32 v[14:15], s[16:17]
	v_mad_u64_u32 v[14:15], s[0:1], v12, s5, v[14:15]
	v_mad_i32_i24 v15, v13, s5, v15
	v_lshl_add_u64 v[12:13], v[14:15], 0, v[2:3]
	s_mov_b32 s0, 0xf800000
	s_waitcnt vmcnt(33)
	v_lshlrev_b32_e32 v41, 16, v17
	v_lshlrev_b32_e32 v40, 16, v16
	s_waitcnt vmcnt(32)
	v_lshlrev_b32_e32 v65, 16, v19
	v_lshlrev_b32_e32 v64, 16, v18
	v_and_b32_e32 v17, 0xffff0000, v17
	v_and_b32_e32 v16, 0xffff0000, v16
	v_and_b32_e32 v19, 0xffff0000, v19
	v_and_b32_e32 v18, 0xffff0000, v18
	s_waitcnt vmcnt(29)
	v_lshlrev_b32_e32 v95, 16, v31
	v_lshlrev_b32_e32 v94, 16, v30
	s_waitcnt vmcnt(28)
	v_lshlrev_b32_e32 v97, 16, v35
	v_lshlrev_b32_e32 v96, 16, v34
	v_and_b32_e32 v31, 0xffff0000, v31
	v_and_b32_e32 v30, 0xffff0000, v30
	v_and_b32_e32 v35, 0xffff0000, v35
	v_and_b32_e32 v34, 0xffff0000, v34
	v_pk_fma_f32 v[72:73], v[214:215], v[18:19], v[16:17] neg_lo:[1,0,0] neg_hi:[1,0,0]
	v_pk_fma_f32 v[18:19], v[214:215], v[96:97], v[94:95] neg_lo:[1,0,0] neg_hi:[1,0,0]
	v_pk_fma_f32 v[16:17], v[214:215], v[34:35], v[30:31] neg_lo:[1,0,0] neg_hi:[1,0,0]
	v_lshlrev_b32_e32 v71, 16, v25
	v_lshlrev_b32_e32 v70, 16, v24
	v_lshlrev_b32_e32 v93, 16, v27
	v_lshlrev_b32_e32 v92, 16, v26
	v_and_b32_e32 v25, 0xffff0000, v25
	v_and_b32_e32 v24, 0xffff0000, v24
	v_and_b32_e32 v27, 0xffff0000, v27
	v_and_b32_e32 v26, 0xffff0000, v26
	v_mov_b32_e32 v30, v18
	v_mov_b32_e32 v31, v16
	v_mul_f32_e32 v34, v16, v16
	v_pk_fma_f32 v[78:79], v[214:215], v[64:65], v[40:41] neg_lo:[1,0,0] neg_hi:[1,0,0]
	v_pk_fma_f32 v[64:65], v[214:215], v[26:27], v[24:25] neg_lo:[1,0,0] neg_hi:[1,0,0]
	v_pk_fma_f32 v[30:31], v[30:31], v[30:31], v[34:35] op_sel_hi:[1,1,0]
	v_mov_b32_e32 v34, v19
	v_mov_b32_e32 v35, v17
	v_mul_f32_e32 v40, v17, v17
	v_pk_fma_f32 v[70:71], v[214:215], v[92:93], v[70:71] neg_lo:[1,0,0] neg_hi:[1,0,0]
	v_pk_mul_f32 v[24:25], v[72:73], v[72:73]
	v_pk_mul_f32 v[26:27], v[64:65], v[64:65]
	v_pk_fma_f32 v[34:35], v[34:35], v[34:35], v[40:41] op_sel_hi:[1,1,0]
	s_waitcnt vmcnt(27)
	v_lshlrev_b32_e32 v41, 16, v43
	v_lshlrev_b32_e32 v40, 16, v42
	s_waitcnt vmcnt(26)
	v_lshlrev_b32_e32 v93, 16, v51
	v_lshlrev_b32_e32 v92, 16, v50
	v_and_b32_e32 v43, 0xffff0000, v43
	v_and_b32_e32 v42, 0xffff0000, v42
	v_and_b32_e32 v51, 0xffff0000, v51
	v_and_b32_e32 v50, 0xffff0000, v50
	v_pk_fma_f32 v[24:25], v[78:79], v[78:79], v[24:25]
	v_pk_fma_f32 v[26:27], v[70:71], v[70:71], v[26:27]
	v_pk_fma_f32 v[40:41], v[214:215], v[92:93], v[40:41] neg_lo:[1,0,0] neg_hi:[1,0,0]
	v_pk_fma_f32 v[50:51], v[214:215], v[50:51], v[42:43] neg_lo:[1,0,0] neg_hi:[1,0,0]
	v_pk_add_f32 v[24:25], v[24:25], v[24:25] op_sel:[0,1] op_sel_hi:[1,0]
	v_pk_add_f32 v[26:27], v[26:27], v[26:27] op_sel:[0,1] op_sel_hi:[1,0]
	v_pk_mul_f32 v[42:43], v[40:41], v[40:41]
	v_pk_mul_f32 v[92:93], v[50:51], v[50:51]
	v_mov_b32_e32 v25, v42
	v_mov_b32_e32 v27, v92
	v_mov_b32_e32 v31, v43
	v_mov_b32_e32 v35, v93
	v_pk_add_f32 v[24:25], v[24:25], v[26:27]
	v_pk_add_f32 v[26:27], v[30:31], v[34:35]
	s_waitcnt vmcnt(24)
	v_and_b32_e32 v31, 0xffff0000, v61
	v_pk_add_f32 v[24:25], v[24:25], v[26:27]
	v_lshlrev_b32_e32 v27, 16, v61
	v_pk_add_f32 v[92:93], v[24:25], v[24:25] op_sel:[0,1] op_sel_hi:[1,0]
	v_lshlrev_b32_e32 v25, 16, v55
	v_lshlrev_b32_e32 v24, 16, v54
	v_lshlrev_b32_e32 v26, 16, v60
	v_pk_fma_f32 v[26:27], v[214:215], v[26:27], v[24:25] neg_lo:[1,0,0] neg_hi:[1,0,0]
	v_and_b32_e32 v25, 0xffff0000, v55
	v_and_b32_e32 v24, 0xffff0000, v54
	v_and_b32_e32 v30, 0xffff0000, v60
	v_pk_fma_f32 v[34:35], v[214:215], v[30:31], v[24:25] neg_lo:[1,0,0] neg_hi:[1,0,0]
	s_waitcnt vmcnt(22)
	v_lshlrev_b32_e32 v31, 16, v85
	v_pk_mul_f32 v[24:25], v[34:35], v[34:35]
	v_lshlrev_b32_e32 v30, 16, v84
	v_pk_fma_f32 v[24:25], v[26:27], v[26:27], v[24:25]
	s_waitcnt vmcnt(0)
	v_mov_b32_e32 v15, v10
	v_pk_add_f32 v[60:61], v[24:25], v[24:25] op_sel:[0,1] op_sel_hi:[1,0]
	v_lshlrev_b32_e32 v25, 16, v75
	v_lshlrev_b32_e32 v24, 16, v74
	v_pk_fma_f32 v[42:43], v[214:215], v[30:31], v[24:25] neg_lo:[1,0,0] neg_hi:[1,0,0]
	v_and_b32_e32 v25, 0xffff0000, v75
	v_and_b32_e32 v24, 0xffff0000, v74
	v_and_b32_e32 v31, 0xffff0000, v85
	v_and_b32_e32 v30, 0xffff0000, v84
	v_pk_fma_f32 v[54:55], v[214:215], v[30:31], v[24:25] neg_lo:[1,0,0] neg_hi:[1,0,0]
	v_mov_b32_e32 v24, v42
	v_mov_b32_e32 v25, v54
	v_mul_f32_e32 v30, v54, v54
	v_pk_fma_f32 v[74:75], v[24:25], v[24:25], v[30:31] op_sel_hi:[1,1,0]
	v_mov_b32_e32 v24, v43
	v_mov_b32_e32 v25, v55
	v_mul_f32_e32 v30, v55, v55
	v_pk_fma_f32 v[84:85], v[24:25], v[24:25], v[30:31] op_sel_hi:[1,1,0]
	v_lshlrev_b32_e32 v25, 16, v87
	v_lshlrev_b32_e32 v24, 16, v86
	v_lshlrev_b32_e32 v31, 16, v89
	v_lshlrev_b32_e32 v30, 16, v88
	v_pk_fma_f32 v[24:25], v[214:215], v[30:31], v[24:25] neg_lo:[1,0,0] neg_hi:[1,0,0]
	v_and_b32_e32 v31, 0xffff0000, v87
	v_and_b32_e32 v30, 0xffff0000, v86
	v_and_b32_e32 v87, 0xffff0000, v89
	v_and_b32_e32 v86, 0xffff0000, v88
	v_pk_fma_f32 v[30:31], v[214:215], v[86:87], v[30:31] neg_lo:[1,0,0] neg_hi:[1,0,0]
	v_pk_mul_f32 v[86:87], v[24:25], v[24:25]
	v_pk_mul_f32 v[88:89], v[30:31], v[30:31]
	v_mov_b32_e32 v93, v86
	v_mov_b32_e32 v61, v88
	v_mov_b32_e32 v75, v87
	v_mov_b32_e32 v85, v89
	v_pk_add_f32 v[60:61], v[92:93], v[60:61]
	v_pk_add_f32 v[74:75], v[74:75], v[84:85]
	v_lshlrev_b32_e32 v89, 16, v37
	v_pk_add_f32 v[60:61], v[60:61], v[74:75]
	v_lshlrev_b32_e32 v75, 16, v29
	v_pk_add_f32 v[84:85], v[60:61], v[60:61] op_sel:[0,1] op_sel_hi:[1,0]
	v_lshlrev_b32_e32 v61, 16, v91
	v_lshlrev_b32_e32 v60, 16, v90
	v_lshlrev_b32_e32 v74, 16, v28
	v_pk_fma_f32 v[60:61], v[214:215], v[74:75], v[60:61] neg_lo:[1,0,0] neg_hi:[1,0,0]
	v_and_b32_e32 v75, 0xffff0000, v91
	v_and_b32_e32 v74, 0xffff0000, v90
	v_and_b32_e32 v29, 0xffff0000, v29
	v_and_b32_e32 v28, 0xffff0000, v28
	v_pk_fma_f32 v[74:75], v[214:215], v[28:29], v[74:75] neg_lo:[1,0,0] neg_hi:[1,0,0]
	v_lshlrev_b32_e32 v88, 16, v36
	v_pk_mul_f32 v[28:29], v[74:75], v[74:75]
	v_and_b32_e32 v37, 0xffff0000, v37
	v_pk_fma_f32 v[28:29], v[60:61], v[60:61], v[28:29]
	v_and_b32_e32 v36, 0xffff0000, v36
	v_pk_add_f32 v[86:87], v[28:29], v[28:29] op_sel:[0,1] op_sel_hi:[1,0]
	v_lshlrev_b32_e32 v29, 16, v59
	v_lshlrev_b32_e32 v28, 16, v58
	v_and_b32_e32 v59, 0xffff0000, v59
	v_and_b32_e32 v58, 0xffff0000, v58
	v_pk_fma_f32 v[28:29], v[214:215], v[88:89], v[28:29] neg_lo:[1,0,0] neg_hi:[1,0,0]
	v_pk_fma_f32 v[36:37], v[214:215], v[36:37], v[58:59] neg_lo:[1,0,0] neg_hi:[1,0,0]
	v_mov_b32_e32 v58, v28
	v_mov_b32_e32 v59, v36
	v_mul_f32_e32 v88, v36, v36
	v_pk_fma_f32 v[88:89], v[58:59], v[58:59], v[88:89] op_sel_hi:[1,1,0]
	v_mov_b32_e32 v58, v29
	v_mov_b32_e32 v59, v37
	v_mul_f32_e32 v90, v37, v37
	v_pk_fma_f32 v[90:91], v[58:59], v[58:59], v[90:91] op_sel_hi:[1,1,0]
	v_lshlrev_b32_e32 v59, 16, v67
	v_lshlrev_b32_e32 v58, 16, v66
	v_lshlrev_b32_e32 v93, 16, v45
	v_lshlrev_b32_e32 v92, 16, v44
	v_and_b32_e32 v67, 0xffff0000, v67
	v_and_b32_e32 v66, 0xffff0000, v66
	v_and_b32_e32 v45, 0xffff0000, v45
	v_and_b32_e32 v44, 0xffff0000, v44
	v_pk_fma_f32 v[58:59], v[214:215], v[92:93], v[58:59] neg_lo:[1,0,0] neg_hi:[1,0,0]
	v_pk_fma_f32 v[66:67], v[214:215], v[44:45], v[66:67] neg_lo:[1,0,0] neg_hi:[1,0,0]
	v_pk_mul_f32 v[44:45], v[58:59], v[58:59]
	v_pk_mul_f32 v[92:93], v[66:67], v[66:67]
	v_mov_b32_e32 v85, v44
	v_mov_b32_e32 v87, v92
	v_mov_b32_e32 v89, v45
	v_mov_b32_e32 v91, v93
	v_pk_add_f32 v[84:85], v[84:85], v[86:87]
	v_pk_add_f32 v[44:45], v[88:89], v[90:91]
	v_lshlrev_b32_e32 v87, 16, v53
	v_pk_add_f32 v[44:45], v[84:85], v[44:45]
	v_lshlrev_b32_e32 v86, 16, v52
	v_pk_add_f32 v[84:85], v[44:45], v[44:45] op_sel:[0,1] op_sel_hi:[1,0]
	v_lshlrev_b32_e32 v45, 16, v63
	v_lshlrev_b32_e32 v44, 16, v62
	v_and_b32_e32 v63, 0xffff0000, v63
	v_and_b32_e32 v62, 0xffff0000, v62
	v_and_b32_e32 v53, 0xffff0000, v53
	v_and_b32_e32 v52, 0xffff0000, v52
	v_pk_fma_f32 v[52:53], v[214:215], v[52:53], v[62:63] neg_lo:[1,0,0] neg_hi:[1,0,0]
	v_pk_fma_f32 v[44:45], v[214:215], v[86:87], v[44:45] neg_lo:[1,0,0] neg_hi:[1,0,0]
	v_pk_mul_f32 v[62:63], v[52:53], v[52:53]
	v_lshlrev_b32_e32 v89, 16, v33
	v_pk_fma_f32 v[62:63], v[44:45], v[44:45], v[62:63]
	v_lshlrev_b32_e32 v88, 16, v32
	v_pk_add_f32 v[86:87], v[62:63], v[62:63] op_sel:[0,1] op_sel_hi:[1,0]
	v_lshlrev_b32_e32 v63, 16, v77
	v_lshlrev_b32_e32 v62, 16, v76
	v_and_b32_e32 v77, 0xffff0000, v77
	v_and_b32_e32 v76, 0xffff0000, v76
	v_and_b32_e32 v33, 0xffff0000, v33
	v_and_b32_e32 v32, 0xffff0000, v32
	v_pk_fma_f32 v[62:63], v[214:215], v[88:89], v[62:63] neg_lo:[1,0,0] neg_hi:[1,0,0]
	v_pk_fma_f32 v[76:77], v[214:215], v[32:33], v[76:77] neg_lo:[1,0,0] neg_hi:[1,0,0]
	v_mov_b32_e32 v32, v62
	v_mov_b32_e32 v33, v76
	v_mul_f32_e32 v88, v76, v76
	v_pk_fma_f32 v[88:89], v[32:33], v[32:33], v[88:89] op_sel_hi:[1,1,0]
	v_mov_b32_e32 v32, v63
	v_mov_b32_e32 v33, v77
	v_mul_f32_e32 v90, v77, v77
	v_pk_fma_f32 v[90:91], v[32:33], v[32:33], v[90:91] op_sel_hi:[1,1,0]
	v_lshlrev_b32_e32 v33, 16, v69
	v_lshlrev_b32_e32 v32, 16, v68
	v_lshlrev_b32_e32 v93, 16, v39
	v_lshlrev_b32_e32 v92, 16, v38
	v_and_b32_e32 v69, 0xffff0000, v69
	v_and_b32_e32 v68, 0xffff0000, v68
	v_and_b32_e32 v39, 0xffff0000, v39
	v_and_b32_e32 v38, 0xffff0000, v38
	v_pk_fma_f32 v[32:33], v[214:215], v[92:93], v[32:33] neg_lo:[1,0,0] neg_hi:[1,0,0]
	v_pk_fma_f32 v[38:39], v[214:215], v[38:39], v[68:69] neg_lo:[1,0,0] neg_hi:[1,0,0]
	v_pk_mul_f32 v[68:69], v[32:33], v[32:33]
	v_pk_mul_f32 v[92:93], v[38:39], v[38:39]
	v_mov_b32_e32 v85, v68
	v_mov_b32_e32 v87, v92
	v_mov_b32_e32 v89, v69
	v_mov_b32_e32 v91, v93
	v_pk_add_f32 v[84:85], v[84:85], v[86:87]
	v_pk_add_f32 v[68:69], v[88:89], v[90:91]
	v_lshlrev_b32_e32 v87, 16, v21
	v_pk_add_f32 v[68:69], v[84:85], v[68:69]
	v_lshlrev_b32_e32 v86, 16, v20
	v_pk_add_f32 v[84:85], v[68:69], v[68:69] op_sel:[0,1] op_sel_hi:[1,0]
	v_lshlrev_b32_e32 v69, 16, v81
	v_lshlrev_b32_e32 v68, 16, v80
	v_and_b32_e32 v81, 0xffff0000, v81
	v_and_b32_e32 v80, 0xffff0000, v80
	v_and_b32_e32 v21, 0xffff0000, v21
	v_and_b32_e32 v20, 0xffff0000, v20
	v_pk_fma_f32 v[80:81], v[214:215], v[20:21], v[80:81] neg_lo:[1,0,0] neg_hi:[1,0,0]
	v_pk_fma_f32 v[68:69], v[214:215], v[86:87], v[68:69] neg_lo:[1,0,0] neg_hi:[1,0,0]
	v_pk_mul_f32 v[20:21], v[80:81], v[80:81]
	v_lshlrev_b32_e32 v89, 16, v23
	v_pk_fma_f32 v[20:21], v[68:69], v[68:69], v[20:21]
	v_lshlrev_b32_e32 v88, 16, v22
	v_pk_add_f32 v[86:87], v[20:21], v[20:21] op_sel:[0,1] op_sel_hi:[1,0]
	v_lshlrev_b32_e32 v21, 16, v47
	v_lshlrev_b32_e32 v20, 16, v46
	v_and_b32_e32 v47, 0xffff0000, v47
	v_and_b32_e32 v46, 0xffff0000, v46
	v_and_b32_e32 v23, 0xffff0000, v23
	v_and_b32_e32 v22, 0xffff0000, v22
	v_pk_fma_f32 v[20:21], v[214:215], v[88:89], v[20:21] neg_lo:[1,0,0] neg_hi:[1,0,0]
	v_pk_fma_f32 v[22:23], v[214:215], v[22:23], v[46:47] neg_lo:[1,0,0] neg_hi:[1,0,0]
	v_mov_b32_e32 v46, v20
	v_mov_b32_e32 v47, v22
	v_mul_f32_e32 v88, v22, v22
	v_pk_fma_f32 v[88:89], v[46:47], v[46:47], v[88:89] op_sel_hi:[1,1,0]
	v_mov_b32_e32 v46, v21
	v_mov_b32_e32 v47, v23
	v_mul_f32_e32 v90, v23, v23
	v_pk_fma_f32 v[90:91], v[46:47], v[46:47], v[90:91] op_sel_hi:[1,1,0]
	v_lshlrev_b32_e32 v47, 16, v57
	v_lshlrev_b32_e32 v46, 16, v56
	v_lshlrev_b32_e32 v93, 16, v49
	v_lshlrev_b32_e32 v92, 16, v48
	v_and_b32_e32 v57, 0xffff0000, v57
	v_and_b32_e32 v56, 0xffff0000, v56
	v_and_b32_e32 v49, 0xffff0000, v49
	v_and_b32_e32 v48, 0xffff0000, v48
	v_pk_fma_f32 v[46:47], v[214:215], v[92:93], v[46:47] neg_lo:[1,0,0] neg_hi:[1,0,0]
	v_pk_fma_f32 v[48:49], v[214:215], v[48:49], v[56:57] neg_lo:[1,0,0] neg_hi:[1,0,0]
	v_pk_mul_f32 v[56:57], v[46:47], v[46:47]
	v_pk_mul_f32 v[92:93], v[48:49], v[48:49]
	v_mov_b32_e32 v85, v56
	v_mov_b32_e32 v87, v92
	v_mov_b32_e32 v89, v57
	v_mov_b32_e32 v91, v93
	v_pk_add_f32 v[84:85], v[84:85], v[86:87]
	v_pk_add_f32 v[56:57], v[88:89], v[90:91]
	v_mov_b32_e32 v10, v9
	v_pk_add_f32 v[56:57], v[84:85], v[56:57]
	s_nop 0
	v_add_f32_e32 v56, v56, v57
	ds_bpermute_b32 v57, v83, v56
	s_waitcnt lgkmcnt(0)
	v_add_f32_e32 v2, v56, v57
	v_fmamk_f32 v2, v2, 0x3c000000, v1
	v_mul_f32_e32 v14, 0x4f800000, v2
	v_cmp_gt_f32_e32 vcc, s0, v2
	s_nop 1
	v_cndmask_b32_e32 v2, v2, v14, vcc
	v_sqrt_f32_e32 v56, v2
	v_mov_b32_e32 v14, v8
	v_add_u32_e32 v8, -1, v56
	v_fma_f32 v9, -v8, v56, v2
	v_cmp_ge_f32_e64 s[0:1], 0, v9
	v_add_u32_e32 v9, 1, v56
	s_nop 0
	v_cndmask_b32_e64 v8, v56, v8, s[0:1]
	v_fma_f32 v56, -v9, v56, v2
	v_cmp_lt_f32_e64 s[0:1], 0, v56
	s_nop 1
	v_cndmask_b32_e64 v8, v8, v9, s[0:1]
	v_mul_f32_e32 v9, 0x37800000, v8
	v_cndmask_b32_e32 v8, v8, v9, vcc
	v_cmp_class_f32_e32 vcc, v2, v226
	v_mov_b32_e32 v9, v6
	v_mov_b32_e32 v6, v5
	v_cndmask_b32_e32 v2, v8, v2, vcc
	v_div_scale_f32 v56, s[0:1], v2, v2, 1.0
	v_rcp_f32_e32 v57, v56
	v_mov_b32_e32 v8, v4
	v_fma_f32 v4, -v56, v57, 1.0
	v_fmac_f32_e32 v57, v4, v57
	v_div_scale_f32 v4, vcc, 1.0, v2, 1.0
	v_mul_f32_e32 v5, v4, v57
	v_fma_f32 v83, -v56, v5, v4
	v_fmac_f32_e32 v5, v83, v57
	v_fma_f32 v4, -v56, v5, v4
	v_div_fmas_f32 v4, v4, v57, v5
	v_div_fixup_f32 v2, v4, v2, 1.0
	v_mul_f32_e32 v2, 0x3f24fd5c, v2
	v_pk_mul_f32 v[4:5], v[78:79], v[2:3] op_sel_hi:[1,0]
	v_pk_mul_f32 v[16:17], v[16:17], v[2:3] op_sel_hi:[1,0]
	v_pk_mul_f32 v[4:5], v[14:15], v[4:5]
	v_pk_mul_f32 v[14:15], v[72:73], v[2:3] op_sel_hi:[1,0]
	s_nop 0
	v_pk_mul_f32 v[10:11], v[10:11], v[14:15]
	v_pk_mul_f32 v[14:15], v[70:71], v[2:3] op_sel_hi:[1,0]
	v_pk_mul_f32 v[8:9], v[8:9], v[14:15]
	v_pk_mul_f32 v[14:15], v[64:65], v[2:3] op_sel_hi:[1,0]
	v_pk_mul_f32 v[6:7], v[6:7], v[14:15]
	v_cvt_pk_bf16_f32 v7, v9, v7
	v_cvt_pk_bf16_f32 v6, v8, v6
	v_cvt_pk_bf16_f32 v5, v5, v11
	v_cvt_pk_bf16_f32 v4, v4, v10
	global_store_dwordx4 v[12:13], v[4:7], off offset:1024
	global_load_dwordx4 v[4:7], v82, s[58:59] offset:544
	s_nop 0
	global_load_dwordx4 v[8:11], v82, s[58:59] offset:560
	v_pk_mul_f32 v[14:15], v[18:19], v[2:3] op_sel_hi:[1,0]
	s_waitcnt vmcnt(1)
	v_mov_b32_e32 v19, v6
	v_mov_b32_e32 v6, v5
	v_mov_b32_e32 v18, v4
	v_pk_mul_f32 v[4:5], v[6:7], v[16:17]
	v_pk_mul_f32 v[6:7], v[40:41], v[2:3] op_sel_hi:[1,0]
	s_waitcnt vmcnt(0)
	v_mov_b32_e32 v16, v8
	v_mov_b32_e32 v17, v10
	v_pk_mul_f32 v[6:7], v[16:17], v[6:7]
	v_pk_mul_f32 v[16:17], v[50:51], v[2:3] op_sel_hi:[1,0]
	v_mov_b32_e32 v10, v9
	v_pk_mul_f32 v[8:9], v[10:11], v[16:17]
	v_pk_mul_f32 v[14:15], v[18:19], v[14:15]
	v_bfe_u32 v10, v9, 16, 1
	v_bfe_u32 v11, v8, 16, 1
	v_add3_u32 v8, v8, v11, s62
	v_add3_u32 v9, v9, v10, s62
	v_bfe_u32 v16, v6, 16, 1
	v_bfe_u32 v17, v7, 16, 1
	v_add3_u32 v7, v7, v17, s62
	v_add3_u32 v6, v6, v16, s62
	v_lshrrev_b32_e32 v6, 16, v6
	v_lshrrev_b32_e32 v7, 16, v7
	v_and_or_b32 v7, v9, s61, v7
	v_and_or_b32 v6, v8, s61, v6
	v_cvt_pk_bf16_f32 v5, v15, v5
	v_cvt_pk_bf16_f32 v4, v14, v4
	global_store_dwordx4 v[12:13], v[4:7], off offset:1040
	global_load_dwordx4 v[4:7], v82, s[58:59] offset:576
	s_nop 0
	global_load_dwordx4 v[8:11], v82, s[58:59] offset:592
	v_pk_mul_f32 v[14:15], v[26:27], v[2:3] op_sel_hi:[1,0]
	v_pk_mul_f32 v[18:19], v[62:63], v[2:3] op_sel_hi:[1,0]
	s_waitcnt vmcnt(1)
	v_mov_b32_e32 v16, v4
	v_mov_b32_e32 v17, v6
	v_pk_mul_f32 v[14:15], v[14:15], v[16:17]
	v_pk_mul_f32 v[16:17], v[34:35], v[2:3] op_sel_hi:[1,0]
	v_mov_b32_e32 v6, v5
	v_pk_mul_f32 v[4:5], v[16:17], v[6:7]
	v_pk_mul_f32 v[6:7], v[42:43], v[2:3] op_sel_hi:[1,0]
	s_waitcnt vmcnt(0)
	v_mov_b32_e32 v16, v8
	v_mov_b32_e32 v17, v10
	v_pk_mul_f32 v[6:7], v[6:7], v[16:17]
	v_pk_mul_f32 v[16:17], v[54:55], v[2:3] op_sel_hi:[1,0]
	v_mov_b32_e32 v10, v9
	v_pk_mul_f32 v[8:9], v[16:17], v[10:11]
	v_bfe_u32 v10, v9, 16, 1
	v_bfe_u32 v11, v8, 16, 1
	v_add3_u32 v8, v8, v11, s62
	v_add3_u32 v9, v9, v10, s62
	v_bfe_u32 v16, v6, 16, 1
	v_bfe_u32 v17, v7, 16, 1
	v_add3_u32 v7, v7, v17, s62
	v_add3_u32 v6, v6, v16, s62
	v_lshrrev_b32_e32 v6, 16, v6
	v_lshrrev_b32_e32 v7, 16, v7
	v_and_or_b32 v7, v9, s61, v7
	v_and_or_b32 v6, v8, s61, v6
	v_cvt_pk_bf16_f32 v5, v15, v5
	v_cvt_pk_bf16_f32 v4, v14, v4
	global_store_dwordx4 v[12:13], v[4:7], off offset:1056
	global_load_dwordx4 v[4:7], v82, s[58:59] offset:608
	s_nop 0
	global_load_dwordx4 v[8:11], v82, s[58:59] offset:624
	v_pk_mul_f32 v[14:15], v[24:25], v[2:3] op_sel_hi:[1,0]
	v_pk_mul_f32 v[24:25], v[76:77], v[2:3] op_sel_hi:[1,0]
	s_waitcnt vmcnt(1)
	v_mov_b32_e32 v16, v4
	v_mov_b32_e32 v17, v6
	v_pk_mul_f32 v[14:15], v[14:15], v[16:17]
	v_pk_mul_f32 v[16:17], v[30:31], v[2:3] op_sel_hi:[1,0]
	v_mov_b32_e32 v6, v5
	v_pk_mul_f32 v[4:5], v[16:17], v[6:7]
	v_pk_mul_f32 v[6:7], v[60:61], v[2:3] op_sel_hi:[1,0]
	s_waitcnt vmcnt(0)
	v_mov_b32_e32 v16, v8
	v_mov_b32_e32 v17, v10
	v_pk_mul_f32 v[6:7], v[6:7], v[16:17]
	v_pk_mul_f32 v[16:17], v[74:75], v[2:3] op_sel_hi:[1,0]
	v_mov_b32_e32 v10, v9
	v_pk_mul_f32 v[8:9], v[16:17], v[10:11]
	v_bfe_u32 v10, v9, 16, 1
	v_bfe_u32 v11, v8, 16, 1
	v_add3_u32 v8, v8, v11, s62
	v_add3_u32 v9, v9, v10, s62
	v_bfe_u32 v16, v6, 16, 1
	v_bfe_u32 v17, v7, 16, 1
	v_add3_u32 v7, v7, v17, s62
	v_add3_u32 v6, v6, v16, s62
	v_lshrrev_b32_e32 v6, 16, v6
	v_lshrrev_b32_e32 v7, 16, v7
	v_and_or_b32 v7, v9, s61, v7
	v_and_or_b32 v6, v8, s61, v6
	v_cvt_pk_bf16_f32 v5, v15, v5
	v_cvt_pk_bf16_f32 v4, v14, v4
	global_store_dwordx4 v[12:13], v[4:7], off offset:1072
	global_load_dwordx4 v[4:7], v82, s[58:59] offset:640
	s_nop 0
	global_load_dwordx4 v[8:11], v82, s[58:59] offset:656
	v_pk_mul_f32 v[14:15], v[28:29], v[2:3] op_sel_hi:[1,0]
	s_waitcnt vmcnt(1)
	v_mov_b32_e32 v16, v4
	v_mov_b32_e32 v17, v6
	v_pk_mul_f32 v[14:15], v[14:15], v[16:17]
	v_pk_mul_f32 v[16:17], v[36:37], v[2:3] op_sel_hi:[1,0]
	v_mov_b32_e32 v6, v5
	v_pk_mul_f32 v[4:5], v[16:17], v[6:7]
	v_pk_mul_f32 v[6:7], v[58:59], v[2:3] op_sel_hi:[1,0]
	s_waitcnt vmcnt(0)
	v_mov_b32_e32 v16, v8
	v_mov_b32_e32 v17, v10
	v_pk_mul_f32 v[6:7], v[6:7], v[16:17]
	v_pk_mul_f32 v[16:17], v[66:67], v[2:3] op_sel_hi:[1,0]
	v_mov_b32_e32 v10, v9
	v_pk_mul_f32 v[8:9], v[16:17], v[10:11]
	v_bfe_u32 v10, v9, 16, 1
	v_bfe_u32 v11, v8, 16, 1
	v_add3_u32 v8, v8, v11, s62
	v_add3_u32 v9, v9, v10, s62
	v_bfe_u32 v16, v6, 16, 1
	v_bfe_u32 v17, v7, 16, 1
	v_add3_u32 v7, v7, v17, s62
	v_add3_u32 v6, v6, v16, s62
	v_lshrrev_b32_e32 v6, 16, v6
	v_lshrrev_b32_e32 v7, 16, v7
	v_and_or_b32 v7, v9, s61, v7
	v_and_or_b32 v6, v8, s61, v6
	v_cvt_pk_bf16_f32 v5, v15, v5
	v_cvt_pk_bf16_f32 v4, v14, v4
	global_store_dwordx4 v[12:13], v[4:7], off offset:1088
	global_load_dwordx4 v[4:7], v82, s[58:59] offset:672
	s_nop 0
	global_load_dwordx4 v[8:11], v82, s[58:59] offset:688
	v_pk_mul_f32 v[16:17], v[52:53], v[2:3] op_sel_hi:[1,0]
	v_pk_mul_f32 v[14:15], v[44:45], v[2:3] op_sel_hi:[1,0]
	s_waitcnt vmcnt(1)
	v_mov_b32_e32 v27, v6
	v_mov_b32_e32 v6, v5
	s_waitcnt vmcnt(0)
	v_mov_b32_e32 v5, v10
	v_mov_b32_e32 v10, v9
	v_mov_b32_e32 v26, v4
	v_mov_b32_e32 v4, v8
	v_pk_mul_f32 v[6:7], v[16:17], v[6:7]
	v_pk_mul_f32 v[10:11], v[24:25], v[10:11]
	v_pk_mul_f32 v[8:9], v[14:15], v[26:27]
	v_pk_mul_f32 v[4:5], v[18:19], v[4:5]
	v_bfe_u32 v14, v11, 16, 1
	v_bfe_u32 v15, v10, 16, 1
	v_bfe_u32 v16, v7, 16, 1
	v_bfe_u32 v17, v6, 16, 1
	v_add3_u32 v17, v6, v17, s62
	v_add3_u32 v16, v7, v16, s62
	v_add3_u32 v6, v10, v15, s62
	v_add3_u32 v7, v11, v14, s62
	v_bfe_u32 v10, v8, 16, 1
	v_bfe_u32 v11, v9, 16, 1
	v_bfe_u32 v14, v4, 16, 1
	v_bfe_u32 v15, v5, 16, 1
	v_add3_u32 v5, v5, v15, s62
	v_add3_u32 v4, v4, v14, s62
	v_add3_u32 v9, v9, v11, s62
	v_add3_u32 v8, v8, v10, s62
	v_lshrrev_b32_e32 v8, 16, v8
	v_lshrrev_b32_e32 v9, 16, v9
	v_lshrrev_b32_e32 v4, 16, v4
	v_lshrrev_b32_e32 v5, 16, v5
	v_and_or_b32 v7, v7, s61, v5
	v_and_or_b32 v6, v6, s61, v4
	v_and_or_b32 v5, v16, s61, v9
	v_and_or_b32 v4, v17, s61, v8
	global_store_dwordx4 v[12:13], v[4:7], off offset:1104
	global_load_dwordx4 v[4:7], v82, s[58:59] offset:704
	s_nop 0
	global_load_dwordx4 v[8:11], v82, s[58:59] offset:720
	v_pk_mul_f32 v[14:15], v[32:33], v[2:3] op_sel_hi:[1,0]
	v_pk_mul_f32 v[18:19], v[68:69], v[2:3] op_sel_hi:[1,0]
	v_pk_mul_f32 v[16:17], v[38:39], v[2:3] op_sel_hi:[1,0]
	v_pk_mul_f32 v[24:25], v[80:81], v[2:3] op_sel_hi:[1,0]
	s_waitcnt vmcnt(1)
	v_mov_b32_e32 v26, v4
	v_mov_b32_e32 v27, v6
	v_mov_b32_e32 v6, v5
	s_waitcnt vmcnt(0)
	v_mov_b32_e32 v4, v8
	v_mov_b32_e32 v5, v10
	v_mov_b32_e32 v10, v9
	v_pk_mul_f32 v[8:9], v[14:15], v[26:27]
	v_pk_mul_f32 v[4:5], v[18:19], v[4:5]
	v_pk_mul_f32 v[6:7], v[16:17], v[6:7]
	v_pk_mul_f32 v[10:11], v[24:25], v[10:11]
	v_bfe_u32 v18, v8, 16, 1
	v_bfe_u32 v19, v9, 16, 1
	v_bfe_u32 v16, v7, 16, 1
	v_bfe_u32 v17, v6, 16, 1
	v_add3_u32 v9, v9, v19, s62
	v_add3_u32 v8, v8, v18, s62
	v_add3_u32 v17, v6, v17, s62
	v_add3_u32 v16, v7, v16, s62
	v_lshrrev_b32_e32 v8, 16, v8
	v_lshrrev_b32_e32 v9, 16, v9
	v_cvt_pk_bf16_f32 v7, v5, v11
	v_cvt_pk_bf16_f32 v6, v4, v10
	v_and_or_b32 v5, v16, s61, v9
	v_and_or_b32 v4, v17, s61, v8
	global_store_dwordx4 v[12:13], v[4:7], off offset:1120
	global_load_dwordx4 v[4:7], v82, s[58:59] offset:736
	s_nop 0
	global_load_dwordx4 v[8:11], v82, s[58:59] offset:752
	v_pk_mul_f32 v[14:15], v[20:21], v[2:3] op_sel_hi:[1,0]
	v_pk_mul_f32 v[16:17], v[22:23], v[2:3] op_sel_hi:[1,0]
	v_pk_mul_f32 v[18:19], v[46:47], v[2:3] op_sel_hi:[1,0]
	v_pk_mul_f32 v[20:21], v[48:49], v[2:3] op_sel_hi:[1,0]
	s_waitcnt vmcnt(1)
	v_mov_b32_e32 v22, v4
	v_mov_b32_e32 v23, v6
	v_mov_b32_e32 v6, v5
	s_waitcnt vmcnt(0)
	v_mov_b32_e32 v4, v8
	v_mov_b32_e32 v5, v10
	v_mov_b32_e32 v10, v9
	v_pk_mul_f32 v[8:9], v[14:15], v[22:23]
	v_pk_mul_f32 v[6:7], v[16:17], v[6:7]
	v_pk_mul_f32 v[4:5], v[18:19], v[4:5]
	v_pk_mul_f32 v[10:11], v[20:21], v[10:11]
	v_bfe_u32 v15, v7, 16, 1
	v_bfe_u32 v17, v8, 16, 1
	v_bfe_u32 v18, v9, 16, 1
	v_bfe_u32 v19, v4, 16, 1
	v_bfe_u32 v14, v10, 16, 1
	v_bfe_u32 v16, v6, 16, 1
	v_add3_u32 v15, v7, v15, s62
	v_add3_u32 v4, v4, v19, s62
	v_add3_u32 v7, v9, v18, s62
	v_add3_u32 v8, v8, v17, s62
	v_add3_u32 v16, v6, v16, s62
	v_add3_u32 v6, v10, v14, s62
	v_lshrrev_b32_e32 v8, 16, v8
	v_lshrrev_b32_e32 v9, 16, v7
	v_lshrrev_b32_e32 v4, 16, v4
	v_cvt_pk_bf16_f32 v7, v5, v11
	v_and_or_b32 v6, v6, s61, v4
	v_and_or_b32 v5, v15, s61, v9
	v_and_or_b32 v4, v16, s61, v8
	global_store_dwordx4 v[12:13], v[4:7], off offset:1136
	s_branch .LBB0_872
.LBB0_959:
	v_max_f32_e32 v16, v16, v16
	v_max_f32_e32 v17, 0, v16
	v_exp_f32_e64 v16, -v17
	v_cmp_gt_u32_e32 vcc, 32, v230
	s_and_saveexec_b64 s[2:3], vcc
	ds_write_b32 v235, v16
	s_or_b64 exec, exec, s[2:3]
	v_sub_f32_e32 v113, v113, v17
	v_sub_f32_e32 v112, v112, v17
	v_sub_f32_e32 v111, v111, v17
	v_sub_f32_e32 v110, v110, v17
	v_sub_f32_e32 v109, v109, v17
	v_sub_f32_e32 v108, v108, v17
	v_sub_f32_e32 v107, v107, v17
	v_sub_f32_e32 v106, v106, v17
	v_sub_f32_e32 v105, v105, v17
	v_sub_f32_e32 v104, v104, v17
	v_sub_f32_e32 v103, v103, v17
	v_sub_f32_e32 v102, v102, v17
	v_sub_f32_e32 v101, v101, v17
	v_sub_f32_e32 v100, v100, v17
	v_sub_f32_e32 v99, v99, v17
	v_sub_f32_e32 v98, v98, v17
	v_sub_f32_e32 v97, v97, v17
	v_sub_f32_e32 v96, v96, v17
	v_sub_f32_e32 v95, v95, v17
	v_sub_f32_e32 v94, v94, v17
	v_sub_f32_e32 v93, v93, v17
	v_sub_f32_e32 v92, v92, v17
	v_sub_f32_e32 v91, v91, v17
	v_sub_f32_e32 v90, v90, v17
	v_sub_f32_e32 v89, v89, v17
	v_sub_f32_e32 v88, v88, v17
	v_sub_f32_e32 v87, v87, v17
	v_sub_f32_e32 v86, v86, v17
	v_sub_f32_e32 v85, v85, v17
	v_sub_f32_e32 v84, v84, v17
	v_sub_f32_e32 v83, v83, v17
	v_sub_f32_e32 v82, v82, v17
	v_mul_f32_e32 v243, v243, v16
	s_branch .LBB0_953
	s_nop 0
	s_nop 0
	s_nop 0
	s_nop 0
	s_nop 0
	s_nop 0
	s_nop 0
.LBB0_962:
	v_mov_b32_e32 v52, v0
	s_barrier
	s_ashr_i32 s21, s20, 31
	v_readfirstlane_b32 s0, v52
	s_ashr_i32 s2, s0, 2
	s_and_b32 s29, s2, -16
	s_ashr_i32 s3, s0, 7
	v_lshlrev_b32_e32 v2, 4, v52
	v_and_b32_e32 v38, 48, v52
	v_mov_b32_e32 v39, 0
	v_and_b32_e32 v59, 48, v2
	v_lshl_add_u64 v[2:3], s[14:15], 0, v[38:39]
	s_mov_b64 s[0:1], 0x120000
	s_cmp_gt_i32 s3, -1
	v_lshl_add_u64 v[42:43], v[2:3], 0, s[0:1]
	s_cselect_b64 s[0:1], -1, 0
	s_cmp_gt_i32 s3, 0
	v_ashrrev_i32_e32 v58, 2, v52
	s_cselect_b64 s[16:17], -1, 0
	s_cmp_gt_i32 s3, 1
	s_movk_i32 s4, 0x1200
	v_and_b32_e32 v1, 63, v52
	s_cselect_b64 s[18:19], -1, 0
	s_cmp_gt_i32 s3, 2
	v_bfi_b32 v44, -16, s2, v52
	v_mad_i64_i32 v[2:3], s[2:3], v58, s4, 0
	v_mov_b32_e32 v8, 0x90000
	v_lshlrev_b32_e32 v1, 2, v1
	v_mad_i64_i32 v[2:3], s[2:3], s20, v8, v[2:3]
	v_xor_b32_e32 v45, 4, v1
	v_xor_b32_e32 v53, 8, v1
	s_cselect_b64 s[22:23], -1, 0
	v_and_b32_e32 v1, 3, v52
	s_add_u32 s2, s94, s46
	v_lshl_or_b32 v2, v1, 5, v2
	s_addc_u32 s3, s95, 0
	v_bfe_u32 v41, v52, 4, 2
	v_lshl_add_u64 v[46:47], s[2:3], 0, v[2:3]
	v_mad_i64_i32 v[2:3], s[4:5], v44, s4, 0
	v_lshlrev_b32_e32 v40, 3, v41
	v_mad_i64_i32 v[2:3], s[4:5], s20, v8, v[2:3]
	v_or_b32_e32 v2, v2, v40
	v_and_b32_e32 v55, 15, v52
	v_lshl_add_u64 v[2:3], s[2:3], 0, v[2:3]
	s_mov_b64 s[2:3], 0x10a00040
	v_lshl_add_u32 v4, v58, 1, 0
	v_add_u32_e32 v5, 0, v38
	v_mul_u32_u24_e32 v6, 0x110, v59
	v_mul_u32_u24_e32 v7, 0x110, v55
	v_lshl_add_u64 v[48:49], v[2:3], 0, s[2:3]
	v_cndmask_b32_e64 v2, 0, 1, s[0:1]
	s_mov_b64 s[24:25], 0
	s_mov_b64 s[26:27], 0x10a00200
	v_mov_b32_e32 v39, 0x3727c5ac
	s_mov_b32 s28, 0xf800000
	v_mov_b32_e32 v54, 0x260
	s_movk_i32 s30, 0x7fff
	v_add_u32_e32 v56, v4, v6
	v_cmp_ne_u32_e64 s[2:3], 1, v2
	v_add_u32_e32 v57, v5, v7
	v_mov_b32_e32 v60, 1
	v_readlane_b32 s51, v254, 39
	s_branch .LBB0_964
